# rt14 + NSA block-mask union lane^32 hops via v_permlane32_swap (3 more sites)
# speedup vs baseline: 1.0018x; 1.0018x over previous
; #define LAS __attribute__((address_space(3)))
; #define NSA_YL() ({ int lx_ = lane; asm volatile("" : "+v"(lx_)); (LAS float*)(lds + L_Y) + w * 2048 + lx_; })
; __device__ __forceinline__ void nsa_mfma_phase(Frame& F, int l, bf16* YC, int ypitch) {
;     ...
;         __syncthreads();
;         unsigned long long mymask = 0ull, uni_wg, uni_w;
;         { int lm = lane; asm volatile("" : "+v"(lm)); const unsigned long long ml = MASK[lm]; unsigned lo = (unsigned)ml, hi = (unsigned)(ml >> 32); unsigned lo2 = ((lane >> 5) == (w & 1)) ? lo : 0u, hi2 = ((lane >> 5) == (w & 1)) ? hi : 0u;
; #pragma unroll
;             for (int ofs = 1; ofs < 64; ofs <<= 1) { lo |= __shfl_xor(lo, ofs); hi |= __shfl_xor(hi, ofs); lo2 |= __shfl_xor(lo2, ofs); hi2 |= __shfl_xor(hi2, ofs); }
;             const unsigned long long causal = (c == 63) ? ~0ull : ((2ull << c) - 1ull);
;             uni_wg = (((unsigned long long)(unsigned)__builtin_amdgcn_readfirstlane(hi) << 32) | (unsigned)__builtin_amdgcn_readfirstlane(lo)) & causal;
;             uni_w = (((unsigned long long)(unsigned)__builtin_amdgcn_readfirstlane(hi2) << 32) | (unsigned)__builtin_amdgcn_readfirstlane(lo2)) & causal;
;             (void)mymask; }
;         { float g0; { int lg_ = lane; asm volatile("" : "+v"(lg_)); g0 = ((LAS float*)(lds + L_GT))[w * 192 + lg_]; }
;             LAS float* YL = NSA_YL();
; #pragma unroll
;             for (int i = 0; i < 16; ++i) { YL[64 * i] = g0 * o[0][i]; YL[64 * (16 + i)] = g0 * o[1][i]; } }
;         asm volatile("s_waitcnt vmcnt(0)" ::: "memory");
;         {
;             m = -INFINITY; lsum = 0.f;
; #pragma unroll
;             for (int i = 0; i < 16; ++i) { o[0][i] = 0.f; o[1][i] = 0.f; }
;             unsigned long long rem = uni_wg;
;             int j = 63 - __builtin_clzll(rem); rem &= ~(1ull << j);
;             NSA_ISSUE(0, zb + (size_t)(64 * j) * NZ + Z_KS + g * 64, zb + (size_t)(64 * j) * NZ + Z_VS + g * 64, loffZ);
;             int jn = -1;
;             if (rem) { jn = 63 - __builtin_clzll(rem); rem &= ~(1ull << jn); NSA_ISSUE(1, zb + (size_t)(64 * jn) * NZ + Z_KS + g * 64, zb + (size_t)(64 * jn) * NZ + Z_VS + g * 64, loffZ); }
.LBB0_514:
	v_mov_b32_e32 v0, v123
	s_waitcnt lgkmcnt(0)
	s_barrier
	v_xor_b32_e32 v37, 1, v228
	v_lshl_add_u32 v0, v0, 3, 0
	v_add_u32_e32 v0, 0x1c400, v0
	ds_read_b64 v[34:35], v0
	v_cmp_lt_i32_e32 vcc, v37, v90
	v_readlane_b32 s0, v246, 26
	v_readlane_b32 s1, v246, 27
	v_cndmask_b32_e32 v37, v228, v37, vcc
	v_lshlrev_b32_e32 v37, 2, v37
	s_waitcnt lgkmcnt(0)
	ds_bpermute_b32 v38, v37, v34
	v_cndmask_b32_e64 v0, 0, v34, s[0:1]
	v_cndmask_b32_e64 v36, 0, v35, s[0:1]
	s_mul_i32 s78, s78, 0x6e00000
	s_add_u32 s62, s50, s78
	s_waitcnt lgkmcnt(0)
	v_or_b32_e32 v34, v38, v34
	ds_bpermute_b32 v38, v37, v35
	s_addc_u32 s63, s51, 0
	s_lshl_b64 s[0:1], 2, s70
	s_add_u32 s5, s0, -1
	s_addc_u32 s8, s1, -1
	s_waitcnt lgkmcnt(0)
	v_or_b32_e32 v35, v38, v35
	ds_bpermute_b32 v38, v37, v0
	ds_bpermute_b32 v37, v37, v36
	s_cmp_lg_u32 s70, 63
	s_cselect_b32 s11, s8, -1
	s_cselect_b32 s10, s5, -1
	s_waitcnt lgkmcnt(1)
	v_or_b32_e32 v0, v38, v0
	s_waitcnt lgkmcnt(0)
	v_or_b32_e32 v36, v37, v36
	v_xor_b32_e32 v37, 2, v228
	v_cmp_lt_i32_e32 vcc, v37, v90
	s_mov_b64 s[42:43], 0x3400
	s_mov_b64 s[44:45], 0x3600
	v_cndmask_b32_e32 v37, v228, v37, vcc
	v_lshlrev_b32_e32 v37, 2, v37
	ds_bpermute_b32 v38, v37, v34
	s_mov_b32 s64, -1
	s_waitcnt lgkmcnt(0)
	v_or_b32_e32 v34, v38, v34
	ds_bpermute_b32 v38, v37, v35
	s_waitcnt lgkmcnt(0)
	v_or_b32_e32 v35, v38, v35
	ds_bpermute_b32 v38, v37, v0
	ds_bpermute_b32 v37, v37, v36
	s_waitcnt lgkmcnt(1)
	v_or_b32_e32 v0, v38, v0
	s_waitcnt lgkmcnt(0)
	v_or_b32_e32 v36, v37, v36
	v_xor_b32_e32 v37, 4, v228
	v_cmp_lt_i32_e32 vcc, v37, v90
	s_nop 1
	v_cndmask_b32_e32 v37, v228, v37, vcc
	v_lshlrev_b32_e32 v37, 2, v37
	ds_bpermute_b32 v38, v37, v34
	s_waitcnt lgkmcnt(0)
	v_or_b32_e32 v34, v38, v34
	ds_bpermute_b32 v38, v37, v35
	s_waitcnt lgkmcnt(0)
	v_or_b32_e32 v35, v38, v35
	ds_bpermute_b32 v38, v37, v0
	ds_bpermute_b32 v37, v37, v36
	s_waitcnt lgkmcnt(1)
	v_or_b32_e32 v0, v38, v0
	s_waitcnt lgkmcnt(0)
	v_or_b32_e32 v36, v37, v36
	v_xor_b32_e32 v37, 8, v228
	v_cmp_lt_i32_e32 vcc, v37, v90
	s_nop 1
	v_cndmask_b32_e32 v37, v228, v37, vcc
	v_lshlrev_b32_e32 v37, 2, v37
	ds_bpermute_b32 v38, v37, v34
	s_waitcnt lgkmcnt(0)
	v_or_b32_e32 v34, v38, v34
	ds_bpermute_b32 v38, v37, v35
	s_waitcnt lgkmcnt(0)
	v_or_b32_e32 v35, v38, v35
	ds_bpermute_b32 v38, v37, v0
	ds_bpermute_b32 v37, v37, v36
	s_waitcnt lgkmcnt(1)
	v_or_b32_e32 v0, v38, v0
	s_waitcnt lgkmcnt(0)
	v_or_b32_e32 v36, v37, v36
	v_xor_b32_e32 v37, 16, v228
	v_cmp_lt_i32_e32 vcc, v37, v90
	s_nop 1
	v_cndmask_b32_e32 v37, v228, v37, vcc
	v_lshlrev_b32_e32 v37, 2, v37
	ds_bpermute_b32 v38, v37, v34
	s_waitcnt lgkmcnt(0)
	v_or_b32_e32 v34, v38, v34
	ds_bpermute_b32 v38, v37, v35
	s_waitcnt lgkmcnt(0)
	v_or_b32_e32 v35, v38, v35
	ds_bpermute_b32 v38, v37, v0
	ds_bpermute_b32 v37, v37, v36
	s_waitcnt lgkmcnt(1)
	v_or_b32_e32 v0, v38, v0
	s_waitcnt lgkmcnt(0)
	v_or_b32_e32 v36, v37, v36
	v_mov_b32_e32 v37, v34
	s_nop 1
	v_permlane32_swap_b32_e32 v34, v37
	s_waitcnt lgkmcnt(0)
	v_or_b32_e32 v34, v37, v34
	v_mov_b32_e32 v37, v35
	s_nop 1
	v_permlane32_swap_b32_e32 v35, v37
	v_readfirstlane_b32 s2, v34
	v_mov_b32_e32 v34, v123
	s_waitcnt lgkmcnt(0)
	v_or_b32_e32 v35, v37, v35
	v_mov_b32_e32 v37, v0
	s_nop 1
	v_permlane32_swap_b32_e32 v0, v37
	v_readfirstlane_b32 s3, v35
	s_and_b64 s[2:3], s[2:3], s[10:11]
	s_flbit_i32_b64 s5, s[2:3]
	s_xor_b32 s8, s5, 63
	s_waitcnt lgkmcnt(0)
	v_or_b32_e32 v0, v37, v0
	s_lshl_b64 s[12:13], 1, s8
	v_readfirstlane_b32 s0, v0
	v_mov_b32_e32 v0, v123
	s_andn2_b64 s[12:13], s[2:3], s[12:13]
	v_lshl_add_u32 v0, v0, 2, s73
	ds_read_b32 v0, v0
	s_mul_i32 s2, s8, 0x1b8000
	v_lshl_add_u32 v34, v34, 2, s41
	s_add_u32 s9, s62, s2
	s_waitcnt lgkmcnt(0)
	v_mul_f32_e32 v2, v2, v0
	v_mul_f32_e32 v3, v3, v0
	v_mul_f32_e32 v18, v18, v0
	ds_write2st64_b32 v34, v2, v3 offset0:192 offset1:193
	v_mul_f32_e32 v2, v19, v0
	ds_write2st64_b32 v34, v18, v2 offset0:208 offset1:209
	v_mul_f32_e32 v2, v4, v0
	v_mul_f32_e32 v4, v5, v0
	v_mul_f32_e32 v3, v20, v0
	ds_write2st64_b32 v34, v2, v4 offset0:194 offset1:195
	v_mul_f32_e32 v2, v21, v0
	ds_write2st64_b32 v34, v3, v2 offset0:210 offset1:211
	v_mul_f32_e32 v2, v6, v0
	v_mul_f32_e32 v4, v7, v0
	v_mul_f32_e32 v3, v22, v0
	ds_write2st64_b32 v34, v2, v4 offset0:196 offset1:197
	v_mul_f32_e32 v2, v23, v0
	ds_write2st64_b32 v34, v3, v2 offset0:212 offset1:213
	v_mul_f32_e32 v2, v8, v0
	v_mul_f32_e32 v4, v9, v0
	v_mul_f32_e32 v3, v24, v0
	ds_write2st64_b32 v34, v2, v4 offset0:198 offset1:199
	v_mul_f32_e32 v2, v25, v0
	ds_write2st64_b32 v34, v3, v2 offset0:214 offset1:215
	v_mul_f32_e32 v2, v10, v0
	v_mul_f32_e32 v4, v11, v0
	v_mul_f32_e32 v3, v26, v0
	ds_write2st64_b32 v34, v2, v4 offset0:200 offset1:201
	v_mul_f32_e32 v2, v27, v0
	ds_write2st64_b32 v34, v3, v2 offset0:216 offset1:217
	v_mul_f32_e32 v2, v12, v0
	v_mul_f32_e32 v4, v13, v0
	v_mul_f32_e32 v3, v28, v0
	ds_write2st64_b32 v34, v2, v4 offset0:202 offset1:203
	v_mul_f32_e32 v2, v29, v0
	s_addc_u32 s16, s63, 0
	s_lshl_b32 s2, s4, 6
	ds_write2st64_b32 v34, v3, v2 offset0:218 offset1:219
	v_mul_f32_e32 v2, v14, v0
	v_mul_f32_e32 v4, v15, v0
	s_ashr_i32 s3, s2, 31
	v_mul_f32_e32 v3, v30, v0
	ds_write2st64_b32 v34, v2, v4 offset0:204 offset1:205
	v_mul_f32_e32 v2, v31, v0
	s_lshl_b64 s[4:5], s[2:3], 1
	ds_bpermute_b32 v37, v115, v36
	ds_write2st64_b32 v34, v3, v2 offset0:220 offset1:221
	v_mul_f32_e32 v2, v16, v0
	v_mul_f32_e32 v3, v32, v0
	v_mul_f32_e32 v4, v17, v0
	v_mul_f32_e32 v0, v33, v0
	s_add_u32 s2, s9, s4
	ds_write2st64_b32 v34, v2, v4 offset0:206 offset1:207
	ds_write2st64_b32 v34, v3, v0 offset0:222 offset1:223
	v_mov_b32_e32 v0, v125
	s_addc_u32 s3, s16, s5
	s_waitcnt vmcnt(0)
	s_waitcnt lgkmcnt(3)
	v_or_b32_e32 v36, v37, v36
	v_lshl_add_u64 v[2:3], s[2:3], 0, v[0:1]
	v_lshl_add_u64 v[4:5], v[2:3], 0, s[42:43]
	s_mov_b32 s2, m0
	s_mov_b32 m0, s49
	s_nop 0
	global_load_lds_dwordx4 v[4:5], off
	s_mov_b32 m0, s2
	v_lshl_add_u64 v[2:3], v[2:3], 0, s[44:45]
	s_mov_b32 s2, m0
	s_mov_b32 m0, s40
	s_nop 0
	global_load_lds_dwordx4 v[2:3], off
	s_mov_b32 m0, s2
	v_readfirstlane_b32 s1, v36
	s_mov_b64 s[2:3], 0
	s_cmp_eq_u64 s[12:13], 0
	s_cbranch_scc1 .LBB0_516
	s_flbit_i32_b64 s2, s[12:13]
	s_xor_b32 s64, s2, 63
	s_lshl_b64 s[2:3], 1, s64
	s_andn2_b64 s[2:3], s[12:13], s[2:3]
	s_mul_i32 s9, s64, 0x1b8000
	s_add_u32 s9, s62, s9
	s_addc_u32 s13, s63, 0
	s_add_u32 s12, s9, s4
	v_mov_b32_e32 v0, v125
	s_addc_u32 s13, s13, s5
	s_add_i32 s9, s49, 0x2000
	v_lshl_add_u64 v[2:3], s[12:13], 0, v[0:1]
	v_lshl_add_u64 v[4:5], v[2:3], 0, s[42:43]
	s_mov_b32 s12, m0
	s_mov_b32 m0, s9
	s_nop 0
	global_load_lds_dwordx4 v[4:5], off
	s_mov_b32 m0, s12
	v_lshl_add_u64 v[2:3], v[2:3], 0, s[44:45]
	s_add_i32 s9, s49, 0x8000
	s_mov_b32 s12, m0
	s_mov_b32 m0, s9
	s_nop 0
	global_load_lds_dwordx4 v[2:3], off
	s_mov_b32 m0, s12
